# speedup vs baseline: 1.0108x; 1.0010x over previous
.LBB0_8:
	s_andn2_saveexec_b64 s[6:7], s[6:7]
	s_cbranch_execz .LBB0_26
	s_load_dwordx2 s[8:9], s[0:1], 0x30
	v_add_u32_e32 v4, 0xfffca000, v2
	v_and_b32_e32 v1, 15, v0
	v_lshrrev_b32_e32 v2, 1, v2
	v_lshrrev_b32_e32 v0, 1, v0
	v_and_b32_e32 v3, 0xe0, v2
	v_and_b32_e32 v0, 24, v0
	v_cmp_gt_u32_e32 vcc, 4, v1
	v_lshlrev_b32_e32 v1, 8, v1
	v_or3_b32 v1, v0, v3, v1
	v_lshrrev_b32_e32 v2, 9, v4
	v_mov_b32_e32 v0, 0
	v_mul_u32_u24_e32 v3, 9, v1
	v_mov_b32_e32 v1, 0
	v_mov_b32_e32 v5, 0
	v_mov_b32_e32 v6, 0
	v_mov_b32_e32 v7, 0
	v_mov_b32_e32 v8, 0
	v_mov_b32_e32 v9, 0
	v_mov_b32_e32 v10, 0
	s_load_dwordx2 s[10:11], s[0:1], 0x58
	s_and_saveexec_b64 s[12:13], vcc
	s_cbranch_execz .Lmyprep_skip
	v_add_lshl_u32 v11, v3, v2, 2
	s_waitcnt lgkmcnt(0)
	global_load_dword v1, v11, s[8:9]
	global_load_dword v0, v11, s[8:9] offset:36
	global_load_dword v6, v11, s[8:9] offset:72
	global_load_dword v5, v11, s[8:9] offset:108
	global_load_dword v8, v11, s[8:9] offset:144
	global_load_dword v7, v11, s[8:9] offset:180
	global_load_dword v10, v11, s[8:9] offset:216
	global_load_dword v9, v11, s[8:9] offset:252
	s_waitcnt vmcnt(0)
	v_cvt_f16_f32_e32 v1, v1
	v_cvt_f16_f32_e32 v0, v0
	v_cvt_f16_f32_e32 v6, v6
	v_cvt_f16_f32_e32 v5, v5
	v_cvt_f16_f32_e32 v8, v8
	v_cvt_f16_f32_e32 v7, v7
	v_cvt_f16_f32_e32 v10, v10
	v_cvt_f16_f32_e32 v9, v9
